# baseline (speedup 1.0000x reference)
.LBB3_24:
	s_or_b64 exec, exec, s[6:7]
	v_lshl_add_u32 v10, v205, 3, 0
	s_waitcnt lgkmcnt(3)
	v_add_u32_e32 v14, 0x10400, v10
	s_waitcnt lgkmcnt(0)
	s_barrier
	ds_read2_b64 v[10:13], v14 offset1:32
	ds_read2_b64 v[28:31], v14 offset0:64 offset1:96
	ds_read2_b64 v[62:65], v14 offset0:128 offset1:160
	ds_read2_b64 v[152:155], v14 offset0:192 offset1:224
	v_add_u32_e32 v14, 0x800, v14
	s_waitcnt lgkmcnt(3)
	v_pk_add_f32 v[10:11], v[10:11], 0 op_sel_hi:[1,0]
	ds_read2_b64 v[156:159], v14 offset1:32
	ds_read2_b64 v[160:163], v14 offset0:64 offset1:96
	ds_read2_b64 v[164:167], v14 offset0:128 offset1:160
	ds_read2_b64 v[168:171], v14 offset0:192 offset1:224
	s_waitcnt lgkmcnt(6)
	v_pk_add_f32 v[10:11], v[10:11], v[28:29]
	s_mov_b32 s6, 0x3b000000
	s_waitcnt lgkmcnt(5)
	v_pk_add_f32 v[10:11], v[10:11], v[62:63]
	s_add_i32 s11, 0, 0x12800
	s_waitcnt lgkmcnt(4)
	v_pk_add_f32 v[10:11], v[10:11], v[152:153]
	s_mov_b32 s10, 0x3e6d3388
	s_waitcnt lgkmcnt(3)
	v_pk_add_f32 v[10:11], v[10:11], v[156:157]
	s_mov_b32 s8, 0xbf3a00e3
	s_waitcnt lgkmcnt(2)
	v_pk_add_f32 v[10:11], v[10:11], v[160:161]
	s_mov_b32 s14, 0xbf38aa3b
	s_waitcnt lgkmcnt(1)
	v_pk_add_f32 v[10:11], v[10:11], v[164:165]
	s_mov_b32 s12, 0x3f35f0e3
	s_waitcnt lgkmcnt(0)
	v_pk_add_f32 v[10:11], v[10:11], v[168:169]
	s_mov_b32 s16, 0x3e027906
	v_pk_mul_f32 v[16:17], v[10:11], s[6:7] op_sel_hi:[1,0]
	s_nop 0
	v_fma_f32 v10, -v16, v16, v17
	v_add_f32_e32 v10, 0x3727c5ac, v10
	v_rsq_f32_e32 v22, v10
	v_pk_add_f32 v[10:11], v[12:13], 0 op_sel_hi:[1,0]
	v_or_b32_e32 v13, v151, v207
	v_pk_add_f32 v[10:11], v[10:11], v[30:31]
	v_lshlrev_b32_e32 v23, 2, v13
	v_pk_add_f32 v[10:11], v[10:11], v[64:65]
	v_add_u32_e32 v15, s11, v23
	v_pk_add_f32 v[10:11], v[10:11], v[154:155]
	v_pk_add_f32 v[146:147], v[146:147], v[16:17] op_sel_hi:[1,0] neg_lo:[0,1] neg_hi:[0,1]
	v_pk_add_f32 v[10:11], v[10:11], v[158:159]
	v_pk_mul_f32 v[146:147], v[146:147], v[22:23] op_sel_hi:[1,0]
	v_pk_add_f32 v[10:11], v[10:11], v[162:163]
	v_lshlrev_b32_e32 v13, 1, v13
	v_pk_add_f32 v[10:11], v[10:11], v[166:167]
	v_pk_add_f32 v[138:139], v[138:139], v[16:17] op_sel_hi:[1,0] neg_lo:[0,1] neg_hi:[0,1]
	v_pk_add_f32 v[10:11], v[10:11], v[170:171]
	v_pk_mul_f32 v[138:139], v[138:139], v[22:23] op_sel_hi:[1,0]
	v_pk_mul_f32 v[10:11], v[10:11], s[6:7] op_sel_hi:[1,0]
	s_add_i32 s7, 0, 0x12000
	v_add_u32_e32 v14, s7, v23
	v_add_u32_e32 v226, s7, v23
	v_add_u32_e32 v227, s11, v23
	ds_read_b128 v[28:31], v14
	ds_read_b128 v[62:65], v15
	v_pk_add_f32 v[14:15], v[148:149], v[16:17] op_sel_hi:[1,0] neg_lo:[0,1] neg_hi:[0,1]
	s_mov_b32 s6, 0x3f07dc22
	v_pk_mul_f32 v[14:15], v[14:15], v[22:23] op_sel_hi:[1,0]
	v_fma_f32 v12, -v10, v10, v11
	s_waitcnt lgkmcnt(0)
	ds_read_b128 v[210:213], v226 offset:32
	ds_read_b128 v[214:217], v227 offset:32
	v_pk_fma_f32 v[32:33], v[28:29], v[14:15], v[62:63]
	v_pk_fma_f32 v[146:147], v[30:31], v[146:147], v[64:65]
	v_and_b32_e32 v15, 0x7fffffff, v33
	v_and_b32_e32 v14, 0x7fffffff, v32
	v_pk_fma_f32 v[14:15], v[14:15], s[10:11], 1.0 op_sel_hi:[1,0,0]
	v_pk_mul_f32 v[154:155], v[32:33], v[32:33]
	v_rcp_f32_e32 v148, v14
	v_rcp_f32_e32 v149, v15
	v_mov_b64_e32 v[14:15], s[8:9]
	v_pk_mul_f32 v[154:155], v[154:155], s[14:15] op_sel_hi:[1,0]
	s_mov_b32 s8, 0xbe11a98e
	v_pk_fma_f32 v[152:153], v[148:149], s[6:7], v[14:15] op_sel_hi:[1,0,0]
	v_exp_f32_e32 v154, v154
	v_pk_fma_f32 v[152:153], v[148:149], v[152:153], s[12:13] op_sel_hi:[1,1,0]
	v_exp_f32_e32 v155, v155
	v_pk_fma_f32 v[152:153], v[148:149], v[152:153], s[8:9] op_sel_hi:[1,1,0]
	v_add_f32_e32 v12, 0x3727c5ac, v12
	v_pk_fma_f32 v[152:153], v[148:149], v[152:153], s[16:17] op_sel_hi:[1,1,0]
	v_cmp_gt_f32_e32 vcc, 0, v33
	v_pk_mul_f32 v[148:149], v[148:149], v[152:153]
	v_rsq_f32_e32 v12, v12
	v_pk_mul_f32 v[148:149], v[154:155], v[148:149]
	v_and_b32_e32 v155, 0x7fffffff, v147
	v_and_b32_e32 v154, 0x7fffffff, v146
	v_pk_fma_f32 v[154:155], v[154:155], s[10:11], 1.0 op_sel_hi:[1,0,0]
	v_pk_mul_f32 v[152:153], v[32:33], v[148:149]
	v_rcp_f32_e32 v154, v154
	v_rcp_f32_e32 v155, v155
	v_pk_fma_f32 v[148:149], v[32:33], v[148:149], v[32:33] neg_lo:[1,0,0] neg_hi:[1,0,0]
	v_pk_add_f32 v[144:145], v[144:145], v[10:11] op_sel_hi:[1,0] neg_lo:[0,1] neg_hi:[0,1]
	v_cndmask_b32_e32 v33, v149, v153, vcc
	v_cmp_gt_f32_e32 vcc, 0, v32
	v_pk_mul_f32 v[144:145], v[144:145], v[12:13] op_sel_hi:[1,0]
	v_add3_u32 v13, 0, v13, v187
	v_cndmask_b32_e32 v32, v148, v152, vcc
	v_pk_mul_f32 v[152:153], v[146:147], v[146:147]
	v_pk_fma_f32 v[148:149], v[154:155], s[6:7], v[14:15] op_sel_hi:[1,0,0]
	v_pk_mul_f32 v[152:153], v[152:153], s[14:15] op_sel_hi:[1,0]
	v_pk_fma_f32 v[148:149], v[154:155], v[148:149], s[12:13] op_sel_hi:[1,1,0]
	v_exp_f32_e32 v152, v152
	v_exp_f32_e32 v153, v153
	v_pk_fma_f32 v[148:149], v[154:155], v[148:149], s[8:9] op_sel_hi:[1,1,0]
	v_pk_fma_f32 v[28:29], v[28:29], v[144:145], v[62:63]
	v_pk_fma_f32 v[148:149], v[154:155], v[148:149], s[16:17] op_sel_hi:[1,1,0]
	v_and_b32_e32 v63, 0x7fffffff, v29
	v_pk_mul_f32 v[148:149], v[154:155], v[148:149]
	v_and_b32_e32 v62, 0x7fffffff, v28
	v_pk_mul_f32 v[148:149], v[152:153], v[148:149]
	v_pk_fma_f32 v[62:63], v[62:63], s[10:11], 1.0 op_sel_hi:[1,0,0]
	v_pk_mul_f32 v[152:153], v[146:147], v[148:149]
	v_pk_fma_f32 v[148:149], v[146:147], v[148:149], v[146:147] neg_lo:[1,0,0] neg_hi:[1,0,0]
	v_cmp_gt_f32_e32 vcc, 0, v147
	v_rcp_f32_e32 v62, v62
	v_rcp_f32_e32 v63, v63
	v_cvt_pk_f16_f32 v32, v32, v33
	v_cndmask_b32_e32 v33, v149, v153, vcc
	v_cmp_gt_f32_e32 vcc, 0, v146
	v_pk_mul_f32 v[144:145], v[28:29], v[28:29]
	v_pk_add_f32 v[142:143], v[142:143], v[10:11] op_sel_hi:[1,0] neg_lo:[0,1] neg_hi:[0,1]
	v_cndmask_b32_e32 v146, v148, v152, vcc
	v_cvt_pk_f16_f32 v33, v146, v33
	ds_write_b64 v13, v[32:33]
	v_pk_fma_f32 v[32:33], v[62:63], s[6:7], v[14:15] op_sel_hi:[1,0,0]
	v_pk_mul_f32 v[144:145], v[144:145], s[14:15] op_sel_hi:[1,0]
	v_pk_fma_f32 v[32:33], v[62:63], v[32:33], s[12:13] op_sel_hi:[1,1,0]
	v_exp_f32_e32 v144, v144
	v_exp_f32_e32 v145, v145
	v_pk_mul_f32 v[142:143], v[142:143], v[12:13] op_sel_hi:[1,0]
	v_pk_fma_f32 v[32:33], v[62:63], v[32:33], s[8:9] op_sel_hi:[1,1,0]
	v_pk_fma_f32 v[30:31], v[30:31], v[142:143], v[64:65]
	v_pk_fma_f32 v[32:33], v[62:63], v[32:33], s[16:17] op_sel_hi:[1,1,0]
	v_and_b32_e32 v65, 0x7fffffff, v31
	v_and_b32_e32 v64, 0x7fffffff, v30
	v_pk_mul_f32 v[32:33], v[62:63], v[32:33]
	v_pk_fma_f32 v[64:65], v[64:65], s[10:11], 1.0 op_sel_hi:[1,0,0]
	v_pk_mul_f32 v[32:33], v[144:145], v[32:33]
	v_rcp_f32_e32 v64, v64
	v_rcp_f32_e32 v65, v65
	v_pk_mul_f32 v[62:63], v[28:29], v[32:33]
	v_pk_fma_f32 v[32:33], v[28:29], v[32:33], v[28:29] neg_lo:[1,0,0] neg_hi:[1,0,0]
	v_cmp_gt_f32_e32 vcc, 0, v29
	v_pk_add_f32 v[136:137], v[136:137], v[10:11] op_sel_hi:[1,0] neg_lo:[0,1] neg_hi:[0,1]
	v_pk_add_f32 v[132:133], v[132:133], v[10:11] op_sel_hi:[1,0] neg_lo:[0,1] neg_hi:[0,1]
	v_cndmask_b32_e32 v29, v33, v63, vcc
	v_cmp_gt_f32_e32 vcc, 0, v28
	v_pk_mul_f32 v[136:137], v[136:137], v[12:13] op_sel_hi:[1,0]
	v_pk_mul_f32 v[132:133], v[132:133], v[12:13] op_sel_hi:[1,0]
	v_cndmask_b32_e32 v28, v32, v62, vcc
	v_pk_mul_f32 v[62:63], v[30:31], v[30:31]
	v_pk_fma_f32 v[32:33], v[64:65], s[6:7], v[14:15] op_sel_hi:[1,0,0]
	v_pk_mul_f32 v[62:63], v[62:63], s[14:15] op_sel_hi:[1,0]
	v_pk_fma_f32 v[32:33], v[64:65], v[32:33], s[12:13] op_sel_hi:[1,1,0]
	v_exp_f32_e32 v62, v62
	v_exp_f32_e32 v63, v63
	v_pk_fma_f32 v[32:33], v[64:65], v[32:33], s[8:9] op_sel_hi:[1,1,0]
	v_cmp_gt_f32_e32 vcc, 0, v31
	v_pk_fma_f32 v[32:33], v[64:65], v[32:33], s[16:17] op_sel_hi:[1,1,0]
	v_cvt_pk_f16_f32 v28, v28, v29
	v_pk_mul_f32 v[32:33], v[64:65], v[32:33]
	v_pk_add_f32 v[130:131], v[130:131], v[16:17] op_sel_hi:[1,0] neg_lo:[0,1] neg_hi:[0,1]
	v_pk_mul_f32 v[32:33], v[62:63], v[32:33]
	v_pk_mul_f32 v[130:131], v[130:131], v[22:23] op_sel_hi:[1,0]
	v_pk_mul_f32 v[62:63], v[30:31], v[32:33]
	v_pk_fma_f32 v[32:33], v[30:31], v[32:33], v[30:31] neg_lo:[1,0,0] neg_hi:[1,0,0]
	v_pk_add_f32 v[60:61], v[60:61], v[10:11] op_sel_hi:[1,0] neg_lo:[0,1] neg_hi:[0,1]
	v_cndmask_b32_e32 v29, v33, v63, vcc
	v_cmp_gt_f32_e32 vcc, 0, v30
	v_pk_mul_f32 v[60:61], v[60:61], v[12:13] op_sel_hi:[1,0]
	v_pk_add_f32 v[58:59], v[58:59], v[10:11] op_sel_hi:[1,0] neg_lo:[0,1] neg_hi:[0,1]
	v_cndmask_b32_e32 v30, v32, v62, vcc
	v_cvt_pk_f16_f32 v29, v30, v29
	ds_write_b64 v13, v[28:29] offset:33280
	v_or_b32_e32 v28, 32, v23
	v_add_u32_e32 v29, s7, v28
	v_add_u32_e32 v32, s11, v28
	v_pk_add_f32 v[32:33], v[140:141], v[16:17] op_sel_hi:[1,0] neg_lo:[0,1] neg_hi:[0,1]
	v_pk_mul_f32 v[58:59], v[58:59], v[12:13] op_sel_hi:[1,0]
	v_pk_mul_f32 v[32:33], v[32:33], v[22:23] op_sel_hi:[1,0]
	v_pk_add_f32 v[54:55], v[54:55], v[16:17] op_sel_hi:[1,0] neg_lo:[0,1] neg_hi:[0,1]
	s_waitcnt lgkmcnt(0)
	ds_read_b128 v[218:221], v226 offset:64
	ds_read_b128 v[222:225], v227 offset:64
	v_pk_fma_f32 v[32:33], v[210:211], v[32:33], v[214:215]
	v_pk_fma_f32 v[138:139], v[212:213], v[138:139], v[216:217]
	v_and_b32_e32 v141, 0x7fffffff, v33
	v_and_b32_e32 v140, 0x7fffffff, v32
	v_pk_fma_f32 v[140:141], v[140:141], s[10:11], 1.0 op_sel_hi:[1,0,0]
	v_pk_mul_f32 v[144:145], v[32:33], v[32:33]
	v_rcp_f32_e32 v140, v140
	v_rcp_f32_e32 v141, v141
	v_pk_mul_f32 v[144:145], v[144:145], s[14:15] op_sel_hi:[1,0]
	v_cmp_gt_f32_e32 vcc, 0, v33
	v_exp_f32_e32 v144, v144
	v_pk_fma_f32 v[142:143], v[140:141], s[6:7], v[14:15] op_sel_hi:[1,0,0]
	v_exp_f32_e32 v145, v145
	v_pk_fma_f32 v[142:143], v[140:141], v[142:143], s[12:13] op_sel_hi:[1,1,0]
	v_pk_fma_f32 v[28:29], v[210:211], v[136:137], v[214:215]
	v_pk_fma_f32 v[142:143], v[140:141], v[142:143], s[8:9] op_sel_hi:[1,1,0]
	v_and_b32_e32 v63, 0x7fffffff, v29
	v_pk_fma_f32 v[142:143], v[140:141], v[142:143], s[16:17] op_sel_hi:[1,1,0]
	v_and_b32_e32 v62, 0x7fffffff, v28
	v_pk_mul_f32 v[140:141], v[140:141], v[142:143]
	v_pk_fma_f32 v[62:63], v[62:63], s[10:11], 1.0 op_sel_hi:[1,0,0]
	v_pk_mul_f32 v[140:141], v[144:145], v[140:141]
	v_and_b32_e32 v145, 0x7fffffff, v139
	v_and_b32_e32 v144, 0x7fffffff, v138
	v_pk_fma_f32 v[144:145], v[144:145], s[10:11], 1.0 op_sel_hi:[1,0,0]
	v_pk_mul_f32 v[142:143], v[32:33], v[140:141]
	v_rcp_f32_e32 v144, v144
	v_rcp_f32_e32 v145, v145
	v_pk_fma_f32 v[140:141], v[32:33], v[140:141], v[32:33] neg_lo:[1,0,0] neg_hi:[1,0,0]
	v_rcp_f32_e32 v62, v62
	v_cndmask_b32_e32 v33, v141, v143, vcc
	v_cmp_gt_f32_e32 vcc, 0, v32
	v_rcp_f32_e32 v63, v63
	v_pk_fma_f32 v[30:31], v[212:213], v[132:133], v[216:217]
	v_cndmask_b32_e32 v32, v140, v142, vcc
	v_pk_mul_f32 v[142:143], v[138:139], v[138:139]
	v_pk_fma_f32 v[140:141], v[144:145], s[6:7], v[14:15] op_sel_hi:[1,0,0]
	v_pk_mul_f32 v[142:143], v[142:143], s[14:15] op_sel_hi:[1,0]
	v_pk_fma_f32 v[140:141], v[144:145], v[140:141], s[12:13] op_sel_hi:[1,1,0]
	v_exp_f32_e32 v142, v142
	v_exp_f32_e32 v143, v143
	v_pk_fma_f32 v[140:141], v[144:145], v[140:141], s[8:9] op_sel_hi:[1,1,0]
	v_cmp_gt_f32_e32 vcc, 0, v139
	v_pk_fma_f32 v[140:141], v[144:145], v[140:141], s[16:17] op_sel_hi:[1,1,0]
	v_cvt_pk_f16_f32 v32, v32, v33
	v_pk_mul_f32 v[140:141], v[144:145], v[140:141]
	v_and_b32_e32 v65, 0x7fffffff, v31
	v_pk_mul_f32 v[140:141], v[142:143], v[140:141]
	v_and_b32_e32 v64, 0x7fffffff, v30
	v_pk_mul_f32 v[142:143], v[138:139], v[140:141]
	v_pk_fma_f32 v[140:141], v[138:139], v[140:141], v[138:139] neg_lo:[1,0,0] neg_hi:[1,0,0]
	v_pk_fma_f32 v[64:65], v[64:65], s[10:11], 1.0 op_sel_hi:[1,0,0]
	v_cndmask_b32_e32 v33, v141, v143, vcc
	v_cmp_gt_f32_e32 vcc, 0, v138
	v_rcp_f32_e32 v64, v64
	v_rcp_f32_e32 v65, v65
	v_cndmask_b32_e32 v136, v140, v142, vcc
	v_cvt_pk_f16_f32 v33, v136, v33
	v_pk_mul_f32 v[136:137], v[28:29], v[28:29]
	ds_write_b64 v13, v[32:33] offset:16
	v_pk_fma_f32 v[32:33], v[62:63], s[6:7], v[14:15] op_sel_hi:[1,0,0]
	v_pk_mul_f32 v[136:137], v[136:137], s[14:15] op_sel_hi:[1,0]
	v_pk_fma_f32 v[32:33], v[62:63], v[32:33], s[12:13] op_sel_hi:[1,1,0]
	v_exp_f32_e32 v136, v136
	v_exp_f32_e32 v137, v137
	v_pk_fma_f32 v[32:33], v[62:63], v[32:33], s[8:9] op_sel_hi:[1,1,0]
	v_cmp_gt_f32_e32 vcc, 0, v29
	v_pk_fma_f32 v[32:33], v[62:63], v[32:33], s[16:17] op_sel_hi:[1,1,0]
	v_pk_mul_f32 v[54:55], v[54:55], v[22:23] op_sel_hi:[1,0]
	v_pk_mul_f32 v[32:33], v[62:63], v[32:33]
	v_pk_add_f32 v[52:53], v[52:53], v[10:11] op_sel_hi:[1,0] neg_lo:[0,1] neg_hi:[0,1]
	v_pk_mul_f32 v[32:33], v[136:137], v[32:33]
	v_pk_mul_f32 v[52:53], v[52:53], v[12:13] op_sel_hi:[1,0]
	v_pk_mul_f32 v[62:63], v[28:29], v[32:33]
	v_pk_fma_f32 v[32:33], v[28:29], v[32:33], v[28:29] neg_lo:[1,0,0] neg_hi:[1,0,0]
	v_pk_add_f32 v[50:51], v[50:51], v[10:11] op_sel_hi:[1,0] neg_lo:[0,1] neg_hi:[0,1]
	v_cndmask_b32_e32 v29, v33, v63, vcc
	v_cmp_gt_f32_e32 vcc, 0, v28
	v_pk_mul_f32 v[50:51], v[50:51], v[12:13] op_sel_hi:[1,0]
	v_pk_add_f32 v[46:47], v[46:47], v[16:17] op_sel_hi:[1,0] neg_lo:[0,1] neg_hi:[0,1]
	v_cndmask_b32_e32 v28, v32, v62, vcc
	v_pk_mul_f32 v[62:63], v[30:31], v[30:31]
	v_pk_fma_f32 v[32:33], v[64:65], s[6:7], v[14:15] op_sel_hi:[1,0,0]
	v_pk_mul_f32 v[62:63], v[62:63], s[14:15] op_sel_hi:[1,0]
	v_pk_fma_f32 v[32:33], v[64:65], v[32:33], s[12:13] op_sel_hi:[1,1,0]
	v_exp_f32_e32 v62, v62
	v_exp_f32_e32 v63, v63
	v_pk_fma_f32 v[32:33], v[64:65], v[32:33], s[8:9] op_sel_hi:[1,1,0]
	v_cmp_gt_f32_e32 vcc, 0, v31
	v_pk_fma_f32 v[32:33], v[64:65], v[32:33], s[16:17] op_sel_hi:[1,1,0]
	v_cvt_pk_f16_f32 v28, v28, v29
	v_pk_mul_f32 v[32:33], v[64:65], v[32:33]
	v_pk_mul_f32 v[46:47], v[46:47], v[22:23] op_sel_hi:[1,0]
	v_pk_mul_f32 v[32:33], v[62:63], v[32:33]
	v_pk_add_f32 v[44:45], v[44:45], v[10:11] op_sel_hi:[1,0] neg_lo:[0,1] neg_hi:[0,1]
	v_pk_mul_f32 v[62:63], v[30:31], v[32:33]
	v_pk_fma_f32 v[32:33], v[30:31], v[32:33], v[30:31] neg_lo:[1,0,0] neg_hi:[1,0,0]
	v_pk_mul_f32 v[44:45], v[44:45], v[12:13] op_sel_hi:[1,0]
	v_cndmask_b32_e32 v29, v33, v63, vcc
	v_cmp_gt_f32_e32 vcc, 0, v30
	v_pk_add_f32 v[42:43], v[42:43], v[10:11] op_sel_hi:[1,0] neg_lo:[0,1] neg_hi:[0,1]
	v_pk_add_f32 v[38:39], v[38:39], v[16:17] op_sel_hi:[1,0] neg_lo:[0,1] neg_hi:[0,1]
	v_cndmask_b32_e32 v30, v32, v62, vcc
	v_cvt_pk_f16_f32 v29, v30, v29
	ds_write_b64 v13, v[28:29] offset:33296
	v_or_b32_e32 v28, 64, v23
	v_add_u32_e32 v29, s7, v28
	v_add_u32_e32 v32, s11, v28
	v_pk_add_f32 v[32:33], v[134:135], v[16:17] op_sel_hi:[1,0] neg_lo:[0,1] neg_hi:[0,1]
	v_pk_mul_f32 v[42:43], v[42:43], v[12:13] op_sel_hi:[1,0]
	v_pk_mul_f32 v[32:33], v[32:33], v[22:23] op_sel_hi:[1,0]
	v_pk_mul_f32 v[38:39], v[38:39], v[22:23] op_sel_hi:[1,0]
	s_waitcnt lgkmcnt(0)
	ds_read_b128 v[210:213], v226 offset:96
	ds_read_b128 v[214:217], v227 offset:96
	v_pk_fma_f32 v[32:33], v[218:219], v[32:33], v[222:223]
	v_pk_fma_f32 v[130:131], v[220:221], v[130:131], v[224:225]
	v_and_b32_e32 v133, 0x7fffffff, v33
	v_and_b32_e32 v132, 0x7fffffff, v32
	v_pk_fma_f32 v[132:133], v[132:133], s[10:11], 1.0 op_sel_hi:[1,0,0]
	v_pk_mul_f32 v[136:137], v[32:33], v[32:33]
	v_rcp_f32_e32 v132, v132
	v_rcp_f32_e32 v133, v133
	v_pk_mul_f32 v[136:137], v[136:137], s[14:15] op_sel_hi:[1,0]
	v_cmp_gt_f32_e32 vcc, 0, v33
	v_exp_f32_e32 v136, v136
	v_pk_fma_f32 v[134:135], v[132:133], s[6:7], v[14:15] op_sel_hi:[1,0,0]
	v_exp_f32_e32 v137, v137
	v_pk_fma_f32 v[134:135], v[132:133], v[134:135], s[12:13] op_sel_hi:[1,1,0]
	v_pk_fma_f32 v[28:29], v[218:219], v[60:61], v[222:223]
	v_pk_fma_f32 v[134:135], v[132:133], v[134:135], s[8:9] op_sel_hi:[1,1,0]
	v_and_b32_e32 v61, 0x7fffffff, v29
	v_pk_fma_f32 v[134:135], v[132:133], v[134:135], s[16:17] op_sel_hi:[1,1,0]
	v_and_b32_e32 v60, 0x7fffffff, v28
	v_pk_mul_f32 v[132:133], v[132:133], v[134:135]
	v_pk_fma_f32 v[60:61], v[60:61], s[10:11], 1.0 op_sel_hi:[1,0,0]
	v_pk_mul_f32 v[132:133], v[136:137], v[132:133]
	v_and_b32_e32 v137, 0x7fffffff, v131
	v_and_b32_e32 v136, 0x7fffffff, v130
	v_pk_fma_f32 v[136:137], v[136:137], s[10:11], 1.0 op_sel_hi:[1,0,0]
	v_pk_mul_f32 v[134:135], v[32:33], v[132:133]
	v_rcp_f32_e32 v136, v136
	v_rcp_f32_e32 v137, v137
	v_pk_fma_f32 v[132:133], v[32:33], v[132:133], v[32:33] neg_lo:[1,0,0] neg_hi:[1,0,0]
	v_rcp_f32_e32 v60, v60
	v_cndmask_b32_e32 v33, v133, v135, vcc
	v_cmp_gt_f32_e32 vcc, 0, v32
	v_rcp_f32_e32 v61, v61
	v_pk_fma_f32 v[30:31], v[220:221], v[58:59], v[224:225]
	v_cndmask_b32_e32 v32, v132, v134, vcc
	v_pk_mul_f32 v[134:135], v[130:131], v[130:131]
	v_pk_fma_f32 v[132:133], v[136:137], s[6:7], v[14:15] op_sel_hi:[1,0,0]
	v_pk_mul_f32 v[134:135], v[134:135], s[14:15] op_sel_hi:[1,0]
	v_pk_fma_f32 v[132:133], v[136:137], v[132:133], s[12:13] op_sel_hi:[1,1,0]
	v_exp_f32_e32 v134, v134
	v_exp_f32_e32 v135, v135
	v_pk_fma_f32 v[132:133], v[136:137], v[132:133], s[8:9] op_sel_hi:[1,1,0]
	v_cmp_gt_f32_e32 vcc, 0, v131
	v_pk_fma_f32 v[132:133], v[136:137], v[132:133], s[16:17] op_sel_hi:[1,1,0]
	v_cvt_pk_f16_f32 v32, v32, v33
	v_pk_mul_f32 v[132:133], v[136:137], v[132:133]
	v_and_b32_e32 v59, 0x7fffffff, v31
	v_pk_mul_f32 v[132:133], v[134:135], v[132:133]
	v_and_b32_e32 v58, 0x7fffffff, v30
	v_pk_mul_f32 v[134:135], v[130:131], v[132:133]
	v_pk_fma_f32 v[132:133], v[130:131], v[132:133], v[130:131] neg_lo:[1,0,0] neg_hi:[1,0,0]
	v_pk_fma_f32 v[58:59], v[58:59], s[10:11], 1.0 op_sel_hi:[1,0,0]
	v_cndmask_b32_e32 v33, v133, v135, vcc
	v_cmp_gt_f32_e32 vcc, 0, v130
	v_rcp_f32_e32 v58, v58
	v_rcp_f32_e32 v59, v59
	v_cndmask_b32_e32 v62, v132, v134, vcc
	v_cvt_pk_f16_f32 v33, v62, v33
	v_pk_mul_f32 v[62:63], v[28:29], v[28:29]
	ds_write_b64 v13, v[32:33] offset:32
	v_pk_fma_f32 v[32:33], v[60:61], s[6:7], v[14:15] op_sel_hi:[1,0,0]
	v_pk_mul_f32 v[62:63], v[62:63], s[14:15] op_sel_hi:[1,0]
	v_pk_fma_f32 v[32:33], v[60:61], v[32:33], s[12:13] op_sel_hi:[1,1,0]
	v_exp_f32_e32 v62, v62
	v_exp_f32_e32 v63, v63
	v_pk_fma_f32 v[32:33], v[60:61], v[32:33], s[8:9] op_sel_hi:[1,1,0]
	v_cmp_gt_f32_e32 vcc, 0, v29
	v_pk_fma_f32 v[32:33], v[60:61], v[32:33], s[16:17] op_sel_hi:[1,1,0]
	v_pk_add_f32 v[36:37], v[36:37], v[10:11] op_sel_hi:[1,0] neg_lo:[0,1] neg_hi:[0,1]
	v_pk_mul_f32 v[32:33], v[60:61], v[32:33]
	v_pk_mul_f32 v[36:37], v[36:37], v[12:13] op_sel_hi:[1,0]
	v_pk_mul_f32 v[32:33], v[62:63], v[32:33]
	v_pk_add_f32 v[34:35], v[34:35], v[10:11] op_sel_hi:[1,0] neg_lo:[0,1] neg_hi:[0,1]
	v_pk_mul_f32 v[60:61], v[28:29], v[32:33]
	v_pk_fma_f32 v[32:33], v[28:29], v[32:33], v[28:29] neg_lo:[1,0,0] neg_hi:[1,0,0]
	v_pk_mul_f32 v[34:35], v[34:35], v[12:13] op_sel_hi:[1,0]
	v_cndmask_b32_e32 v29, v33, v61, vcc
	v_cmp_gt_f32_e32 vcc, 0, v28
	v_pk_add_f32 v[26:27], v[26:27], v[16:17] op_sel_hi:[1,0] neg_lo:[0,1] neg_hi:[0,1]
	v_pk_add_f32 v[24:25], v[24:25], v[16:17] op_sel_hi:[1,0] neg_lo:[0,1] neg_hi:[0,1]
	v_cndmask_b32_e32 v28, v32, v60, vcc
	v_pk_mul_f32 v[60:61], v[30:31], v[30:31]
	v_pk_fma_f32 v[32:33], v[58:59], s[6:7], v[14:15] op_sel_hi:[1,0,0]
	v_pk_mul_f32 v[60:61], v[60:61], s[14:15] op_sel_hi:[1,0]
	v_pk_fma_f32 v[32:33], v[58:59], v[32:33], s[12:13] op_sel_hi:[1,1,0]
	v_exp_f32_e32 v60, v60
	v_exp_f32_e32 v61, v61
	v_pk_fma_f32 v[32:33], v[58:59], v[32:33], s[8:9] op_sel_hi:[1,1,0]
	v_cmp_gt_f32_e32 vcc, 0, v31
	v_pk_fma_f32 v[32:33], v[58:59], v[32:33], s[16:17] op_sel_hi:[1,1,0]
	v_cvt_pk_f16_f32 v28, v28, v29
	v_pk_mul_f32 v[32:33], v[58:59], v[32:33]
	v_pk_mul_f32 v[26:27], v[26:27], v[22:23] op_sel_hi:[1,0]
	v_pk_mul_f32 v[32:33], v[60:61], v[32:33]
	v_pk_mul_f32 v[24:25], v[24:25], v[22:23] op_sel_hi:[1,0]
	v_pk_mul_f32 v[58:59], v[30:31], v[32:33]
	v_pk_fma_f32 v[32:33], v[30:31], v[32:33], v[30:31] neg_lo:[1,0,0] neg_hi:[1,0,0]
	v_pk_add_f32 v[20:21], v[20:21], v[10:11] op_sel_hi:[1,0] neg_lo:[0,1] neg_hi:[0,1]
	v_cndmask_b32_e32 v29, v33, v59, vcc
	v_cmp_gt_f32_e32 vcc, 0, v30
	v_pk_mul_f32 v[20:21], v[20:21], v[12:13] op_sel_hi:[1,0]
	v_pk_add_f32 v[18:19], v[18:19], v[10:11] op_sel_hi:[1,0] neg_lo:[0,1] neg_hi:[0,1]
	v_cndmask_b32_e32 v30, v32, v58, vcc
	v_cvt_pk_f16_f32 v29, v30, v29
	ds_write_b64 v13, v[28:29] offset:33312
	v_or_b32_e32 v28, 0x60, v23
	v_add_u32_e32 v29, s7, v28
	v_add_u32_e32 v32, s11, v28
	v_pk_add_f32 v[32:33], v[56:57], v[16:17] op_sel_hi:[1,0] neg_lo:[0,1] neg_hi:[0,1]
	v_pk_mul_f32 v[18:19], v[18:19], v[12:13] op_sel_hi:[1,0]
	v_pk_mul_f32 v[32:33], v[32:33], v[22:23] op_sel_hi:[1,0]
	v_pk_add_f32 v[8:9], v[8:9], v[16:17] op_sel_hi:[1,0] neg_lo:[0,1] neg_hi:[0,1]
	s_waitcnt lgkmcnt(0)
	ds_read_b128 v[218:221], v226 offset:128
	ds_read_b128 v[222:225], v227 offset:128
	v_pk_fma_f32 v[32:33], v[210:211], v[32:33], v[214:215]
	v_pk_fma_f32 v[54:55], v[212:213], v[54:55], v[216:217]
	v_and_b32_e32 v57, 0x7fffffff, v33
	v_and_b32_e32 v56, 0x7fffffff, v32
	v_pk_fma_f32 v[56:57], v[56:57], s[10:11], 1.0 op_sel_hi:[1,0,0]
	v_pk_mul_f32 v[64:65], v[32:33], v[32:33]
	v_rcp_f32_e32 v56, v56
	v_rcp_f32_e32 v57, v57
	v_pk_mul_f32 v[64:65], v[64:65], s[14:15] op_sel_hi:[1,0]
	v_cmp_gt_f32_e32 vcc, 0, v33
	v_exp_f32_e32 v64, v64
	v_pk_fma_f32 v[62:63], v[56:57], s[6:7], v[14:15] op_sel_hi:[1,0,0]
	v_exp_f32_e32 v65, v65
	v_pk_fma_f32 v[62:63], v[56:57], v[62:63], s[12:13] op_sel_hi:[1,1,0]
	v_pk_fma_f32 v[28:29], v[210:211], v[52:53], v[214:215]
	v_pk_fma_f32 v[62:63], v[56:57], v[62:63], s[8:9] op_sel_hi:[1,1,0]
	v_and_b32_e32 v53, 0x7fffffff, v29
	v_pk_fma_f32 v[62:63], v[56:57], v[62:63], s[16:17] op_sel_hi:[1,1,0]
	v_and_b32_e32 v52, 0x7fffffff, v28
	v_pk_mul_f32 v[56:57], v[56:57], v[62:63]
	v_pk_fma_f32 v[52:53], v[52:53], s[10:11], 1.0 op_sel_hi:[1,0,0]
	v_pk_mul_f32 v[56:57], v[64:65], v[56:57]
	v_and_b32_e32 v65, 0x7fffffff, v55
	v_and_b32_e32 v64, 0x7fffffff, v54
	v_pk_fma_f32 v[64:65], v[64:65], s[10:11], 1.0 op_sel_hi:[1,0,0]
	v_pk_mul_f32 v[62:63], v[32:33], v[56:57]
	v_rcp_f32_e32 v64, v64
	v_rcp_f32_e32 v65, v65
	v_pk_fma_f32 v[56:57], v[32:33], v[56:57], v[32:33] neg_lo:[1,0,0] neg_hi:[1,0,0]
	v_rcp_f32_e32 v52, v52
	v_cndmask_b32_e32 v33, v57, v63, vcc
	v_cmp_gt_f32_e32 vcc, 0, v32
	v_rcp_f32_e32 v53, v53
	v_pk_fma_f32 v[30:31], v[212:213], v[50:51], v[216:217]
	v_cndmask_b32_e32 v32, v56, v62, vcc
	v_pk_mul_f32 v[62:63], v[54:55], v[54:55]
	v_pk_fma_f32 v[56:57], v[64:65], s[6:7], v[14:15] op_sel_hi:[1,0,0]
	v_pk_mul_f32 v[62:63], v[62:63], s[14:15] op_sel_hi:[1,0]
	v_pk_fma_f32 v[56:57], v[64:65], v[56:57], s[12:13] op_sel_hi:[1,1,0]
	v_exp_f32_e32 v62, v62
	v_exp_f32_e32 v63, v63
	v_pk_fma_f32 v[56:57], v[64:65], v[56:57], s[8:9] op_sel_hi:[1,1,0]
	v_cmp_gt_f32_e32 vcc, 0, v55
	v_pk_fma_f32 v[56:57], v[64:65], v[56:57], s[16:17] op_sel_hi:[1,1,0]
	v_cvt_pk_f16_f32 v32, v32, v33
	v_pk_mul_f32 v[56:57], v[64:65], v[56:57]
	v_and_b32_e32 v51, 0x7fffffff, v31
	v_pk_mul_f32 v[56:57], v[62:63], v[56:57]
	v_and_b32_e32 v50, 0x7fffffff, v30
	v_pk_mul_f32 v[62:63], v[54:55], v[56:57]
	v_pk_fma_f32 v[56:57], v[54:55], v[56:57], v[54:55] neg_lo:[1,0,0] neg_hi:[1,0,0]
	v_pk_fma_f32 v[50:51], v[50:51], s[10:11], 1.0 op_sel_hi:[1,0,0]
	v_cndmask_b32_e32 v33, v57, v63, vcc
	v_cmp_gt_f32_e32 vcc, 0, v54
	v_rcp_f32_e32 v50, v50
	v_rcp_f32_e32 v51, v51
	v_cndmask_b32_e32 v54, v56, v62, vcc
	v_cvt_pk_f16_f32 v33, v54, v33
	v_pk_mul_f32 v[54:55], v[28:29], v[28:29]
	ds_write_b64 v13, v[32:33] offset:48
	v_pk_fma_f32 v[32:33], v[52:53], s[6:7], v[14:15] op_sel_hi:[1,0,0]
	v_pk_mul_f32 v[54:55], v[54:55], s[14:15] op_sel_hi:[1,0]
	v_pk_fma_f32 v[32:33], v[52:53], v[32:33], s[12:13] op_sel_hi:[1,1,0]
	v_exp_f32_e32 v54, v54
	v_exp_f32_e32 v55, v55
	v_pk_fma_f32 v[32:33], v[52:53], v[32:33], s[8:9] op_sel_hi:[1,1,0]
	v_cmp_gt_f32_e32 vcc, 0, v29
	v_pk_fma_f32 v[32:33], v[52:53], v[32:33], s[16:17] op_sel_hi:[1,1,0]
	v_pk_add_f32 v[6:7], v[6:7], v[16:17] op_sel_hi:[1,0] neg_lo:[0,1] neg_hi:[0,1]
	v_pk_mul_f32 v[32:33], v[52:53], v[32:33]
	v_pk_add_f32 v[4:5], v[4:5], v[10:11] op_sel_hi:[1,0] neg_lo:[0,1] neg_hi:[0,1]
	v_pk_mul_f32 v[32:33], v[54:55], v[32:33]
	v_pk_mul_f32 v[4:5], v[4:5], v[12:13] op_sel_hi:[1,0]
	v_pk_mul_f32 v[52:53], v[28:29], v[32:33]
	v_pk_fma_f32 v[32:33], v[28:29], v[32:33], v[28:29] neg_lo:[1,0,0] neg_hi:[1,0,0]
	v_pk_add_f32 v[2:3], v[2:3], v[10:11] op_sel_hi:[1,0] neg_lo:[0,1] neg_hi:[0,1]
	v_cndmask_b32_e32 v29, v33, v53, vcc
	v_cmp_gt_f32_e32 vcc, 0, v28
	v_pk_mul_f32 v[2:3], v[2:3], v[12:13] op_sel_hi:[1,0]
	s_nop 0
	v_cndmask_b32_e32 v28, v32, v52, vcc
	v_pk_mul_f32 v[52:53], v[30:31], v[30:31]
	v_pk_fma_f32 v[32:33], v[50:51], s[6:7], v[14:15] op_sel_hi:[1,0,0]
	v_pk_mul_f32 v[52:53], v[52:53], s[14:15] op_sel_hi:[1,0]
	v_pk_fma_f32 v[32:33], v[50:51], v[32:33], s[12:13] op_sel_hi:[1,1,0]
	v_exp_f32_e32 v52, v52
	v_exp_f32_e32 v53, v53
	v_pk_fma_f32 v[32:33], v[50:51], v[32:33], s[8:9] op_sel_hi:[1,1,0]
	v_cmp_gt_f32_e32 vcc, 0, v31
	v_pk_fma_f32 v[32:33], v[50:51], v[32:33], s[16:17] op_sel_hi:[1,1,0]
	v_cvt_pk_f16_f32 v28, v28, v29
	v_pk_mul_f32 v[32:33], v[50:51], v[32:33]
	s_nop 0
	v_pk_mul_f32 v[32:33], v[52:53], v[32:33]
	s_nop 0
	v_pk_mul_f32 v[50:51], v[30:31], v[32:33]
	v_pk_fma_f32 v[32:33], v[30:31], v[32:33], v[30:31] neg_lo:[1,0,0] neg_hi:[1,0,0]
	s_nop 0
	v_cndmask_b32_e32 v29, v33, v51, vcc
	v_cmp_gt_f32_e32 vcc, 0, v30
	s_nop 1
	v_cndmask_b32_e32 v30, v32, v50, vcc
	v_cvt_pk_f16_f32 v29, v30, v29
	ds_write_b64 v13, v[28:29] offset:33328
	v_or_b32_e32 v28, 0x80, v23
	v_add_u32_e32 v29, s7, v28
	v_add_u32_e32 v32, s11, v28
	v_pk_add_f32 v[32:33], v[48:49], v[16:17] op_sel_hi:[1,0] neg_lo:[0,1] neg_hi:[0,1]
	s_waitcnt lgkmcnt(0)
	ds_read_b128 v[210:213], v226 offset:160
	ds_read_b128 v[214:217], v227 offset:160
	v_pk_fma_f32 v[46:47], v[220:221], v[46:47], v[224:225]
	v_pk_mul_f32 v[32:33], v[32:33], v[22:23] op_sel_hi:[1,0]
	v_pk_fma_f32 v[30:31], v[220:221], v[42:43], v[224:225]
	v_pk_fma_f32 v[32:33], v[218:219], v[32:33], v[222:223]
	v_pk_fma_f32 v[28:29], v[218:219], v[44:45], v[222:223]
	v_and_b32_e32 v49, 0x7fffffff, v33
	v_and_b32_e32 v48, 0x7fffffff, v32
	v_pk_fma_f32 v[48:49], v[48:49], s[10:11], 1.0 op_sel_hi:[1,0,0]
	v_pk_mul_f32 v[56:57], v[32:33], v[32:33]
	v_rcp_f32_e32 v48, v48
	v_rcp_f32_e32 v49, v49
	v_pk_mul_f32 v[56:57], v[56:57], s[14:15] op_sel_hi:[1,0]
	v_cmp_gt_f32_e32 vcc, 0, v33
	v_exp_f32_e32 v56, v56
	v_pk_fma_f32 v[54:55], v[48:49], s[6:7], v[14:15] op_sel_hi:[1,0,0]
	v_exp_f32_e32 v57, v57
	v_pk_fma_f32 v[54:55], v[48:49], v[54:55], s[12:13] op_sel_hi:[1,1,0]
	v_and_b32_e32 v45, 0x7fffffff, v29
	v_pk_fma_f32 v[54:55], v[48:49], v[54:55], s[8:9] op_sel_hi:[1,1,0]
	v_and_b32_e32 v44, 0x7fffffff, v28
	v_pk_fma_f32 v[54:55], v[48:49], v[54:55], s[16:17] op_sel_hi:[1,1,0]
	v_pk_fma_f32 v[44:45], v[44:45], s[10:11], 1.0 op_sel_hi:[1,0,0]
	v_pk_mul_f32 v[48:49], v[48:49], v[54:55]
	v_rcp_f32_e32 v44, v44
	v_pk_mul_f32 v[48:49], v[56:57], v[48:49]
	v_and_b32_e32 v57, 0x7fffffff, v47
	v_and_b32_e32 v56, 0x7fffffff, v46
	v_pk_fma_f32 v[56:57], v[56:57], s[10:11], 1.0 op_sel_hi:[1,0,0]
	v_pk_mul_f32 v[54:55], v[32:33], v[48:49]
	v_rcp_f32_e32 v56, v56
	v_rcp_f32_e32 v57, v57
	v_pk_fma_f32 v[48:49], v[32:33], v[48:49], v[32:33] neg_lo:[1,0,0] neg_hi:[1,0,0]
	v_rcp_f32_e32 v45, v45
	v_cndmask_b32_e32 v33, v49, v55, vcc
	v_cmp_gt_f32_e32 vcc, 0, v32
	v_and_b32_e32 v43, 0x7fffffff, v31
	v_and_b32_e32 v42, 0x7fffffff, v30
	v_cndmask_b32_e32 v32, v48, v54, vcc
	v_pk_mul_f32 v[54:55], v[46:47], v[46:47]
	v_pk_fma_f32 v[48:49], v[56:57], s[6:7], v[14:15] op_sel_hi:[1,0,0]
	v_pk_mul_f32 v[54:55], v[54:55], s[14:15] op_sel_hi:[1,0]
	v_pk_fma_f32 v[48:49], v[56:57], v[48:49], s[12:13] op_sel_hi:[1,1,0]
	v_exp_f32_e32 v54, v54
	v_exp_f32_e32 v55, v55
	v_pk_fma_f32 v[48:49], v[56:57], v[48:49], s[8:9] op_sel_hi:[1,1,0]
	v_cmp_gt_f32_e32 vcc, 0, v47
	v_pk_fma_f32 v[48:49], v[56:57], v[48:49], s[16:17] op_sel_hi:[1,1,0]
	v_cvt_pk_f16_f32 v32, v32, v33
	v_pk_mul_f32 v[48:49], v[56:57], v[48:49]
	v_pk_fma_f32 v[42:43], v[42:43], s[10:11], 1.0 op_sel_hi:[1,0,0]
	v_pk_mul_f32 v[48:49], v[54:55], v[48:49]
	v_rcp_f32_e32 v42, v42
	v_pk_mul_f32 v[54:55], v[46:47], v[48:49]
	v_pk_fma_f32 v[48:49], v[46:47], v[48:49], v[46:47] neg_lo:[1,0,0] neg_hi:[1,0,0]
	v_rcp_f32_e32 v43, v43
	v_cndmask_b32_e32 v33, v49, v55, vcc
	v_cmp_gt_f32_e32 vcc, 0, v46
	s_nop 1
	v_cndmask_b32_e32 v46, v48, v54, vcc
	v_cvt_pk_f16_f32 v33, v46, v33
	v_pk_mul_f32 v[46:47], v[28:29], v[28:29]
	ds_write_b64 v13, v[32:33] offset:64
	v_pk_fma_f32 v[32:33], v[44:45], s[6:7], v[14:15] op_sel_hi:[1,0,0]
	v_pk_mul_f32 v[46:47], v[46:47], s[14:15] op_sel_hi:[1,0]
	v_pk_fma_f32 v[32:33], v[44:45], v[32:33], s[12:13] op_sel_hi:[1,1,0]
	v_exp_f32_e32 v46, v46
	v_exp_f32_e32 v47, v47
	v_pk_fma_f32 v[32:33], v[44:45], v[32:33], s[8:9] op_sel_hi:[1,1,0]
	v_cmp_gt_f32_e32 vcc, 0, v29
	v_pk_fma_f32 v[32:33], v[44:45], v[32:33], s[16:17] op_sel_hi:[1,1,0]
	s_nop 0
	v_pk_mul_f32 v[32:33], v[44:45], v[32:33]
	s_nop 0
	v_pk_mul_f32 v[32:33], v[46:47], v[32:33]
	s_nop 0
	v_pk_mul_f32 v[44:45], v[28:29], v[32:33]
	v_pk_fma_f32 v[32:33], v[28:29], v[32:33], v[28:29] neg_lo:[1,0,0] neg_hi:[1,0,0]
	s_nop 0
	v_cndmask_b32_e32 v29, v33, v45, vcc
	v_cmp_gt_f32_e32 vcc, 0, v28
	s_nop 1
	v_cndmask_b32_e32 v28, v32, v44, vcc
	v_pk_mul_f32 v[44:45], v[30:31], v[30:31]
	v_pk_fma_f32 v[32:33], v[42:43], s[6:7], v[14:15] op_sel_hi:[1,0,0]
	v_pk_mul_f32 v[44:45], v[44:45], s[14:15] op_sel_hi:[1,0]
	v_pk_fma_f32 v[32:33], v[42:43], v[32:33], s[12:13] op_sel_hi:[1,1,0]
	v_exp_f32_e32 v44, v44
	v_exp_f32_e32 v45, v45
	v_pk_fma_f32 v[32:33], v[42:43], v[32:33], s[8:9] op_sel_hi:[1,1,0]
	v_cmp_gt_f32_e32 vcc, 0, v31
	v_pk_fma_f32 v[32:33], v[42:43], v[32:33], s[16:17] op_sel_hi:[1,1,0]
	v_cvt_pk_f16_f32 v28, v28, v29
	v_pk_mul_f32 v[32:33], v[42:43], v[32:33]
	s_nop 0
	v_pk_mul_f32 v[32:33], v[44:45], v[32:33]
	s_nop 0
	v_pk_mul_f32 v[42:43], v[30:31], v[32:33]
	v_pk_fma_f32 v[32:33], v[30:31], v[32:33], v[30:31] neg_lo:[1,0,0] neg_hi:[1,0,0]
	s_nop 0
	v_cndmask_b32_e32 v29, v33, v43, vcc
	v_cmp_gt_f32_e32 vcc, 0, v30
	s_nop 1
	v_cndmask_b32_e32 v30, v32, v42, vcc
	v_cvt_pk_f16_f32 v29, v30, v29
	ds_write_b64 v13, v[28:29] offset:33344
	v_or_b32_e32 v28, 0xa0, v23
	v_add_u32_e32 v29, s7, v28
	v_add_u32_e32 v32, s11, v28
	v_pk_add_f32 v[32:33], v[40:41], v[16:17] op_sel_hi:[1,0] neg_lo:[0,1] neg_hi:[0,1]
	s_waitcnt lgkmcnt(0)
	ds_read_b128 v[218:221], v226 offset:192
	ds_read_b128 v[222:225], v227 offset:192
	v_pk_fma_f32 v[38:39], v[212:213], v[38:39], v[216:217]
	v_pk_mul_f32 v[32:33], v[32:33], v[22:23] op_sel_hi:[1,0]
	v_pk_fma_f32 v[30:31], v[212:213], v[34:35], v[216:217]
	v_pk_fma_f32 v[32:33], v[210:211], v[32:33], v[214:215]
	v_pk_fma_f32 v[28:29], v[210:211], v[36:37], v[214:215]
	v_and_b32_e32 v41, 0x7fffffff, v33
	v_and_b32_e32 v40, 0x7fffffff, v32
	v_pk_fma_f32 v[40:41], v[40:41], s[10:11], 1.0 op_sel_hi:[1,0,0]
	v_pk_mul_f32 v[48:49], v[32:33], v[32:33]
	v_rcp_f32_e32 v40, v40
	v_rcp_f32_e32 v41, v41
	v_pk_mul_f32 v[48:49], v[48:49], s[14:15] op_sel_hi:[1,0]
	v_cmp_gt_f32_e32 vcc, 0, v33
	v_exp_f32_e32 v48, v48
	v_pk_fma_f32 v[46:47], v[40:41], s[6:7], v[14:15] op_sel_hi:[1,0,0]
	v_exp_f32_e32 v49, v49
	v_pk_fma_f32 v[46:47], v[40:41], v[46:47], s[12:13] op_sel_hi:[1,1,0]
	v_and_b32_e32 v37, 0x7fffffff, v29
	v_pk_fma_f32 v[46:47], v[40:41], v[46:47], s[8:9] op_sel_hi:[1,1,0]
	v_and_b32_e32 v36, 0x7fffffff, v28
	v_pk_fma_f32 v[46:47], v[40:41], v[46:47], s[16:17] op_sel_hi:[1,1,0]
	v_pk_fma_f32 v[36:37], v[36:37], s[10:11], 1.0 op_sel_hi:[1,0,0]
	v_pk_mul_f32 v[40:41], v[40:41], v[46:47]
	v_rcp_f32_e32 v36, v36
	v_pk_mul_f32 v[40:41], v[48:49], v[40:41]
	v_and_b32_e32 v49, 0x7fffffff, v39
	v_and_b32_e32 v48, 0x7fffffff, v38
	v_pk_fma_f32 v[48:49], v[48:49], s[10:11], 1.0 op_sel_hi:[1,0,0]
	v_pk_mul_f32 v[46:47], v[32:33], v[40:41]
	v_rcp_f32_e32 v48, v48
	v_rcp_f32_e32 v49, v49
	v_pk_fma_f32 v[40:41], v[32:33], v[40:41], v[32:33] neg_lo:[1,0,0] neg_hi:[1,0,0]
	v_rcp_f32_e32 v37, v37
	v_cndmask_b32_e32 v33, v41, v47, vcc
	v_cmp_gt_f32_e32 vcc, 0, v32
	v_and_b32_e32 v35, 0x7fffffff, v31
	v_and_b32_e32 v34, 0x7fffffff, v30
	v_cndmask_b32_e32 v32, v40, v46, vcc
	v_pk_mul_f32 v[46:47], v[38:39], v[38:39]
	v_pk_fma_f32 v[40:41], v[48:49], s[6:7], v[14:15] op_sel_hi:[1,0,0]
	v_pk_mul_f32 v[46:47], v[46:47], s[14:15] op_sel_hi:[1,0]
	v_pk_fma_f32 v[40:41], v[48:49], v[40:41], s[12:13] op_sel_hi:[1,1,0]
	v_exp_f32_e32 v46, v46
	v_exp_f32_e32 v47, v47
	v_pk_fma_f32 v[40:41], v[48:49], v[40:41], s[8:9] op_sel_hi:[1,1,0]
	v_cmp_gt_f32_e32 vcc, 0, v39
	v_pk_fma_f32 v[40:41], v[48:49], v[40:41], s[16:17] op_sel_hi:[1,1,0]
	v_cvt_pk_f16_f32 v32, v32, v33
	v_pk_mul_f32 v[40:41], v[48:49], v[40:41]
	v_pk_fma_f32 v[34:35], v[34:35], s[10:11], 1.0 op_sel_hi:[1,0,0]
	v_pk_mul_f32 v[40:41], v[46:47], v[40:41]
	v_rcp_f32_e32 v34, v34
	v_pk_mul_f32 v[46:47], v[38:39], v[40:41]
	v_pk_fma_f32 v[40:41], v[38:39], v[40:41], v[38:39] neg_lo:[1,0,0] neg_hi:[1,0,0]
	v_rcp_f32_e32 v35, v35
	v_cndmask_b32_e32 v33, v41, v47, vcc
	v_cmp_gt_f32_e32 vcc, 0, v38
	s_nop 1
	v_cndmask_b32_e32 v38, v40, v46, vcc
	v_cvt_pk_f16_f32 v33, v38, v33
	v_pk_mul_f32 v[38:39], v[28:29], v[28:29]
	ds_write_b64 v13, v[32:33] offset:80
	v_pk_fma_f32 v[32:33], v[36:37], s[6:7], v[14:15] op_sel_hi:[1,0,0]
	v_pk_mul_f32 v[38:39], v[38:39], s[14:15] op_sel_hi:[1,0]
	v_pk_fma_f32 v[32:33], v[36:37], v[32:33], s[12:13] op_sel_hi:[1,1,0]
	v_exp_f32_e32 v38, v38
	v_exp_f32_e32 v39, v39
	v_pk_fma_f32 v[32:33], v[36:37], v[32:33], s[8:9] op_sel_hi:[1,1,0]
	v_cmp_gt_f32_e32 vcc, 0, v29
	v_pk_fma_f32 v[32:33], v[36:37], v[32:33], s[16:17] op_sel_hi:[1,1,0]
	s_nop 0
	v_pk_mul_f32 v[32:33], v[36:37], v[32:33]
	s_nop 0
	v_pk_mul_f32 v[32:33], v[38:39], v[32:33]
	s_nop 0
	v_pk_mul_f32 v[36:37], v[28:29], v[32:33]
	v_pk_fma_f32 v[32:33], v[28:29], v[32:33], v[28:29] neg_lo:[1,0,0] neg_hi:[1,0,0]
	s_nop 0
	v_cndmask_b32_e32 v29, v33, v37, vcc
	v_cmp_gt_f32_e32 vcc, 0, v28
	s_nop 1
	v_cndmask_b32_e32 v28, v32, v36, vcc
	v_pk_mul_f32 v[36:37], v[30:31], v[30:31]
	v_pk_fma_f32 v[32:33], v[34:35], s[6:7], v[14:15] op_sel_hi:[1,0,0]
	v_pk_mul_f32 v[36:37], v[36:37], s[14:15] op_sel_hi:[1,0]
	v_pk_fma_f32 v[32:33], v[34:35], v[32:33], s[12:13] op_sel_hi:[1,1,0]
	v_exp_f32_e32 v36, v36
	v_exp_f32_e32 v37, v37
	v_pk_fma_f32 v[32:33], v[34:35], v[32:33], s[8:9] op_sel_hi:[1,1,0]
	v_cmp_gt_f32_e32 vcc, 0, v31
	v_pk_fma_f32 v[32:33], v[34:35], v[32:33], s[16:17] op_sel_hi:[1,1,0]
	v_cvt_pk_f16_f32 v28, v28, v29
	v_pk_mul_f32 v[32:33], v[34:35], v[32:33]
	s_nop 0
	v_pk_mul_f32 v[32:33], v[36:37], v[32:33]
	s_nop 0
	v_pk_mul_f32 v[34:35], v[30:31], v[32:33]
	v_pk_fma_f32 v[32:33], v[30:31], v[32:33], v[30:31] neg_lo:[1,0,0] neg_hi:[1,0,0]
	s_nop 0
	v_cndmask_b32_e32 v29, v33, v35, vcc
	v_cmp_gt_f32_e32 vcc, 0, v30
	s_nop 1
	v_cndmask_b32_e32 v30, v32, v34, vcc
	v_cvt_pk_f16_f32 v29, v30, v29
	ds_write_b64 v13, v[28:29] offset:33360
	v_or_b32_e32 v28, 0xc0, v23
	v_add_u32_e32 v29, s7, v28
	v_add_u32_e32 v32, s11, v28
	s_waitcnt lgkmcnt(0)
	ds_read_b128 v[210:213], v226 offset:224
	ds_read_b128 v[214:217], v227 offset:224
	v_pk_fma_f32 v[26:27], v[218:219], v[26:27], v[222:223]
	s_nop 0
	v_and_b32_e32 v37, 0x7fffffff, v27
	v_and_b32_e32 v36, 0x7fffffff, v26
	v_pk_fma_f32 v[36:37], v[36:37], s[10:11], 1.0 op_sel_hi:[1,0,0]
	v_pk_mul_f32 v[40:41], v[26:27], v[26:27]
	v_rcp_f32_e32 v36, v36
	v_rcp_f32_e32 v37, v37
	v_pk_mul_f32 v[40:41], v[40:41], s[14:15] op_sel_hi:[1,0]
	v_pk_fma_f32 v[24:25], v[220:221], v[24:25], v[224:225]
	v_exp_f32_e32 v40, v40
	v_pk_fma_f32 v[38:39], v[36:37], s[6:7], v[14:15] op_sel_hi:[1,0,0]
	v_exp_f32_e32 v41, v41
	v_pk_fma_f32 v[38:39], v[36:37], v[38:39], s[12:13] op_sel_hi:[1,1,0]
	v_cmp_gt_f32_e32 vcc, 0, v27
	v_pk_fma_f32 v[38:39], v[36:37], v[38:39], s[8:9] op_sel_hi:[1,1,0]
	v_pk_fma_f32 v[20:21], v[218:219], v[20:21], v[222:223]
	v_pk_fma_f32 v[38:39], v[36:37], v[38:39], s[16:17] op_sel_hi:[1,1,0]
	v_and_b32_e32 v29, 0x7fffffff, v21
	v_pk_mul_f32 v[36:37], v[36:37], v[38:39]
	v_and_b32_e32 v28, 0x7fffffff, v20
	v_pk_mul_f32 v[36:37], v[40:41], v[36:37]
	v_and_b32_e32 v41, 0x7fffffff, v25
	v_and_b32_e32 v40, 0x7fffffff, v24
	v_pk_fma_f32 v[40:41], v[40:41], s[10:11], 1.0 op_sel_hi:[1,0,0]
	v_pk_mul_f32 v[38:39], v[26:27], v[36:37]
	v_rcp_f32_e32 v40, v40
	v_rcp_f32_e32 v41, v41
	v_pk_fma_f32 v[36:37], v[26:27], v[36:37], v[26:27] neg_lo:[1,0,0] neg_hi:[1,0,0]
	v_pk_fma_f32 v[28:29], v[28:29], s[10:11], 1.0 op_sel_hi:[1,0,0]
	v_cndmask_b32_e32 v27, v37, v39, vcc
	v_cmp_gt_f32_e32 vcc, 0, v26
	v_rcp_f32_e32 v28, v28
	v_rcp_f32_e32 v29, v29
	v_cndmask_b32_e32 v26, v36, v38, vcc
	v_pk_mul_f32 v[38:39], v[24:25], v[24:25]
	v_pk_fma_f32 v[36:37], v[40:41], s[6:7], v[14:15] op_sel_hi:[1,0,0]
	v_pk_mul_f32 v[38:39], v[38:39], s[14:15] op_sel_hi:[1,0]
	v_pk_fma_f32 v[36:37], v[40:41], v[36:37], s[12:13] op_sel_hi:[1,1,0]
	v_exp_f32_e32 v38, v38
	v_exp_f32_e32 v39, v39
	v_pk_fma_f32 v[36:37], v[40:41], v[36:37], s[8:9] op_sel_hi:[1,1,0]
	v_cmp_gt_f32_e32 vcc, 0, v25
	v_pk_fma_f32 v[36:37], v[40:41], v[36:37], s[16:17] op_sel_hi:[1,1,0]
	v_cvt_pk_f16_f32 v26, v26, v27
	v_pk_mul_f32 v[36:37], v[40:41], v[36:37]
	v_pk_fma_f32 v[18:19], v[220:221], v[18:19], v[224:225]
	v_pk_mul_f32 v[36:37], v[38:39], v[36:37]
	s_nop 0
	v_pk_mul_f32 v[38:39], v[24:25], v[36:37]
	v_pk_fma_f32 v[36:37], v[24:25], v[36:37], v[24:25] neg_lo:[1,0,0] neg_hi:[1,0,0]
	s_nop 0
	v_cndmask_b32_e32 v25, v37, v39, vcc
	v_cmp_gt_f32_e32 vcc, 0, v24
	s_nop 1
	v_cndmask_b32_e32 v24, v36, v38, vcc
	v_cvt_pk_f16_f32 v27, v24, v25
	ds_write_b64 v13, v[26:27] offset:96
	v_pk_fma_f32 v[24:25], v[28:29], s[6:7], v[14:15] op_sel_hi:[1,0,0]
	v_pk_mul_f32 v[26:27], v[20:21], v[20:21]
	v_pk_fma_f32 v[24:25], v[28:29], v[24:25], s[12:13] op_sel_hi:[1,1,0]
	v_pk_mul_f32 v[26:27], v[26:27], s[14:15] op_sel_hi:[1,0]
	v_pk_fma_f32 v[24:25], v[28:29], v[24:25], s[8:9] op_sel_hi:[1,1,0]
	v_exp_f32_e32 v26, v26
	v_exp_f32_e32 v27, v27
	v_pk_fma_f32 v[24:25], v[28:29], v[24:25], s[16:17] op_sel_hi:[1,1,0]
	v_cmp_gt_f32_e32 vcc, 0, v21
	v_pk_mul_f32 v[24:25], v[28:29], v[24:25]
	v_and_b32_e32 v29, 0x7fffffff, v19
	v_and_b32_e32 v28, 0x7fffffff, v18
	v_pk_fma_f32 v[28:29], v[28:29], s[10:11], 1.0 op_sel_hi:[1,0,0]
	v_pk_mul_f32 v[24:25], v[26:27], v[24:25]
	v_rcp_f32_e32 v28, v28
	v_rcp_f32_e32 v29, v29
	v_pk_mul_f32 v[26:27], v[20:21], v[24:25]
	v_pk_fma_f32 v[24:25], v[20:21], v[24:25], v[20:21] neg_lo:[1,0,0] neg_hi:[1,0,0]
	s_nop 0
	v_cndmask_b32_e32 v21, v25, v27, vcc
	v_cmp_gt_f32_e32 vcc, 0, v20
	s_nop 1
	v_cndmask_b32_e32 v20, v24, v26, vcc
	v_pk_mul_f32 v[26:27], v[18:19], v[18:19]
	v_pk_fma_f32 v[24:25], v[28:29], s[6:7], v[14:15] op_sel_hi:[1,0,0]
	v_pk_mul_f32 v[26:27], v[26:27], s[14:15] op_sel_hi:[1,0]
	v_pk_fma_f32 v[24:25], v[28:29], v[24:25], s[12:13] op_sel_hi:[1,1,0]
	v_exp_f32_e32 v26, v26
	v_exp_f32_e32 v27, v27
	v_pk_fma_f32 v[24:25], v[28:29], v[24:25], s[8:9] op_sel_hi:[1,1,0]
	v_cmp_gt_f32_e32 vcc, 0, v19
	v_pk_fma_f32 v[24:25], v[28:29], v[24:25], s[16:17] op_sel_hi:[1,1,0]
	v_cvt_pk_f16_f32 v20, v20, v21
	v_pk_mul_f32 v[24:25], v[28:29], v[24:25]
	s_nop 0
	v_pk_mul_f32 v[24:25], v[26:27], v[24:25]
	s_nop 0
	v_pk_mul_f32 v[26:27], v[18:19], v[24:25]
	v_pk_fma_f32 v[24:25], v[18:19], v[24:25], v[18:19] neg_lo:[1,0,0] neg_hi:[1,0,0]
	s_nop 0
	v_cndmask_b32_e32 v19, v25, v27, vcc
	v_cmp_gt_f32_e32 vcc, 0, v18
	s_nop 1
	v_cndmask_b32_e32 v18, v24, v26, vcc
	v_cvt_pk_f16_f32 v21, v18, v19
	v_or_b32_e32 v18, 0xe0, v23
	ds_write_b64 v13, v[20:21] offset:33376
	v_add_u32_e32 v19, s7, v18
	v_add_u32_e32 v23, s11, v18
	v_pk_mul_f32 v[8:9], v[8:9], v[22:23] op_sel_hi:[1,0]
	v_pk_mul_f32 v[6:7], v[6:7], v[22:23] op_sel_hi:[1,0]
	s_waitcnt lgkmcnt(0)
	v_pk_fma_f32 v[8:9], v[210:211], v[8:9], v[214:215]
	s_nop 0
	v_and_b32_e32 v29, 0x7fffffff, v9
	v_and_b32_e32 v28, 0x7fffffff, v8
	v_pk_fma_f32 v[28:29], v[28:29], s[10:11], 1.0 op_sel_hi:[1,0,0]
	v_pk_mul_f32 v[32:33], v[8:9], v[8:9]
	v_rcp_f32_e32 v28, v28
	v_rcp_f32_e32 v29, v29
	v_pk_mul_f32 v[32:33], v[32:33], s[14:15] op_sel_hi:[1,0]
	v_pk_fma_f32 v[6:7], v[212:213], v[6:7], v[216:217]
	v_exp_f32_e32 v32, v32
	v_pk_fma_f32 v[30:31], v[28:29], s[6:7], v[14:15] op_sel_hi:[1,0,0]
	v_exp_f32_e32 v33, v33
	v_pk_fma_f32 v[30:31], v[28:29], v[30:31], s[12:13] op_sel_hi:[1,1,0]
	v_and_b32_e32 v17, 0x7fffffff, v7
	v_pk_fma_f32 v[30:31], v[28:29], v[30:31], s[8:9] op_sel_hi:[1,1,0]
	v_and_b32_e32 v16, 0x7fffffff, v6
	v_pk_fma_f32 v[30:31], v[28:29], v[30:31], s[16:17] op_sel_hi:[1,1,0]
	v_pk_fma_f32 v[16:17], v[16:17], s[10:11], 1.0 op_sel_hi:[1,0,0]
	v_pk_mul_f32 v[28:29], v[28:29], v[30:31]
	v_rcp_f32_e32 v16, v16
	v_pk_mul_f32 v[28:29], v[32:33], v[28:29]
	v_rcp_f32_e32 v17, v17
	v_pk_mul_f32 v[30:31], v[8:9], v[28:29]
	v_pk_fma_f32 v[28:29], v[8:9], v[28:29], v[8:9] neg_lo:[1,0,0] neg_hi:[1,0,0]
	v_cmp_gt_f32_e32 vcc, 0, v9
	v_pk_fma_f32 v[22:23], v[16:17], s[6:7], v[14:15] op_sel_hi:[1,0,0]
	v_pk_fma_f32 v[4:5], v[210:211], v[4:5], v[214:215]
	v_cndmask_b32_e32 v9, v29, v31, vcc
	v_cmp_gt_f32_e32 vcc, 0, v8
	v_pk_fma_f32 v[22:23], v[16:17], v[22:23], s[12:13] op_sel_hi:[1,1,0]
	v_and_b32_e32 v19, 0x7fffffff, v5
	v_cndmask_b32_e32 v8, v28, v30, vcc
	v_pk_mul_f32 v[28:29], v[6:7], v[6:7]
	v_pk_fma_f32 v[22:23], v[16:17], v[22:23], s[8:9] op_sel_hi:[1,1,0]
	v_pk_mul_f32 v[28:29], v[28:29], s[14:15] op_sel_hi:[1,0]
	v_pk_fma_f32 v[22:23], v[16:17], v[22:23], s[16:17] op_sel_hi:[1,1,0]
	v_exp_f32_e32 v28, v28
	v_exp_f32_e32 v29, v29
	v_pk_mul_f32 v[16:17], v[16:17], v[22:23]
	v_and_b32_e32 v18, 0x7fffffff, v4
	v_cmp_gt_f32_e32 vcc, 0, v7
	v_pk_mul_f32 v[16:17], v[28:29], v[16:17]
	v_pk_fma_f32 v[18:19], v[18:19], s[10:11], 1.0 op_sel_hi:[1,0,0]
	v_pk_mul_f32 v[22:23], v[6:7], v[16:17]
	v_pk_fma_f32 v[16:17], v[6:7], v[16:17], v[6:7] neg_lo:[1,0,0] neg_hi:[1,0,0]
	v_rcp_f32_e32 v18, v18
	v_cndmask_b32_e32 v7, v17, v23, vcc
	v_rcp_f32_e32 v19, v19
	v_cmp_gt_f32_e32 vcc, 0, v6
	v_cvt_pk_f16_f32 v8, v8, v9
	v_pk_fma_f32 v[2:3], v[212:213], v[2:3], v[216:217]
	v_cndmask_b32_e32 v6, v16, v22, vcc
	v_cvt_pk_f16_f32 v9, v6, v7
	ds_write_b64 v13, v[8:9] offset:112
	v_pk_mul_f32 v[8:9], v[4:5], v[4:5]
	v_pk_fma_f32 v[6:7], v[18:19], s[6:7], v[14:15] op_sel_hi:[1,0,0]
	v_pk_mul_f32 v[8:9], v[8:9], s[14:15] op_sel_hi:[1,0]
	v_pk_fma_f32 v[6:7], v[18:19], v[6:7], s[12:13] op_sel_hi:[1,1,0]
	v_exp_f32_e32 v8, v8
	v_exp_f32_e32 v9, v9
	v_pk_fma_f32 v[6:7], v[18:19], v[6:7], s[8:9] op_sel_hi:[1,1,0]
	v_and_b32_e32 v11, 0x7fffffff, v3
	v_pk_fma_f32 v[6:7], v[18:19], v[6:7], s[16:17] op_sel_hi:[1,1,0]
	v_and_b32_e32 v10, 0x7fffffff, v2
	v_pk_mul_f32 v[6:7], v[18:19], v[6:7]
	v_pk_fma_f32 v[10:11], v[10:11], s[10:11], 1.0 op_sel_hi:[1,0,0]
	v_pk_mul_f32 v[6:7], v[8:9], v[6:7]
	v_rcp_f32_e32 v10, v10
	v_rcp_f32_e32 v11, v11
	v_pk_mul_f32 v[8:9], v[4:5], v[6:7]
	v_pk_fma_f32 v[6:7], v[4:5], v[6:7], v[4:5] neg_lo:[1,0,0] neg_hi:[1,0,0]
	v_cmp_gt_f32_e32 vcc, 0, v5
	s_nop 1
	v_cndmask_b32_e32 v5, v7, v9, vcc
	v_cmp_gt_f32_e32 vcc, 0, v4
	s_nop 1
	v_cndmask_b32_e32 v4, v6, v8, vcc
	v_pk_mul_f32 v[8:9], v[2:3], v[2:3]
	v_pk_fma_f32 v[6:7], v[10:11], s[6:7], v[14:15] op_sel_hi:[1,0,0]
	v_pk_mul_f32 v[8:9], v[8:9], s[14:15] op_sel_hi:[1,0]
	v_pk_fma_f32 v[6:7], v[10:11], v[6:7], s[12:13] op_sel_hi:[1,1,0]
	v_exp_f32_e32 v8, v8
	v_exp_f32_e32 v9, v9
	v_pk_fma_f32 v[6:7], v[10:11], v[6:7], s[8:9] op_sel_hi:[1,1,0]
	v_cmp_gt_f32_e32 vcc, 0, v3
	v_pk_fma_f32 v[6:7], v[10:11], v[6:7], s[16:17] op_sel_hi:[1,1,0]
	v_cvt_pk_f16_f32 v4, v4, v5
	v_pk_mul_f32 v[6:7], v[10:11], v[6:7]
	s_nop 0
	v_pk_mul_f32 v[6:7], v[8:9], v[6:7]
	s_nop 0
	v_pk_mul_f32 v[8:9], v[2:3], v[6:7]
	v_pk_fma_f32 v[6:7], v[2:3], v[6:7], v[2:3] neg_lo:[1,0,0] neg_hi:[1,0,0]
	s_nop 0
	v_cndmask_b32_e32 v3, v7, v9, vcc
	v_cmp_gt_f32_e32 vcc, 0, v2
	s_nop 1
	v_cndmask_b32_e32 v2, v6, v8, vcc
	v_cvt_pk_f16_f32 v5, v2, v3
	ds_write_b64 v13, v[4:5] offset:33392
	s_waitcnt lgkmcnt(0)
	s_barrier
	ds_read_b128 v[2:5], v202
	ds_read_b128 v[38:41], v202 offset:32
	ds_read_b128 v[6:9], v202 offset:33280
	ds_read_b128 v[42:45], v202 offset:33312
	s_waitcnt vmcnt(7) lgkmcnt(3)
	v_mfma_f32_32x32x16_f16 v[18:33], v[126:129], v[2:5], 0
	ds_read_b128 v[46:49], v202 offset:64
	ds_read_b128 v[50:53], v202 offset:33344
	ds_read_b128 v[34:37], v204
	s_waitcnt lgkmcnt(4)
	v_mfma_f32_32x32x16_f16 v[2:17], v[126:129], v[6:9], 0
	s_waitcnt vmcnt(6)
	v_mfma_f32_32x32x16_f16 v[18:33], v[122:125], v[38:41], v[18:33]
	ds_read_b128 v[54:57], v202 offset:96
	ds_read_b128 v[58:61], v202 offset:33376
	ds_read_b128 v[38:41], v204 offset:1024
	s_waitcnt lgkmcnt(6)
	v_mfma_f32_32x32x16_f16 v[2:17], v[122:125], v[42:45], v[2:17]
	s_waitcnt vmcnt(5) lgkmcnt(5)
	v_mfma_f32_32x32x16_f16 v[18:33], v[118:121], v[46:49], v[18:33]
	ds_read_b128 v[62:65], v202 offset:128
	ds_read_b128 v[122:125], v202 offset:33408
	ds_read_b128 v[42:45], v204 offset:2048
	s_waitcnt lgkmcnt(7)
	v_mfma_f32_32x32x16_f16 v[2:17], v[118:121], v[50:53], v[2:17]
	s_waitcnt vmcnt(4) lgkmcnt(5)
	v_mfma_f32_32x32x16_f16 v[18:33], v[114:117], v[54:57], v[18:33]
	ds_read_b128 v[50:53], v202 offset:160
	ds_read_b128 v[118:121], v202 offset:33440
	ds_read_b128 v[46:49], v204 offset:3072
	s_waitcnt lgkmcnt(7)
	v_mfma_f32_32x32x16_f16 v[2:17], v[114:117], v[58:61], v[2:17]
	s_waitcnt vmcnt(3) lgkmcnt(5)
	v_mfma_f32_32x32x16_f16 v[18:33], v[110:113], v[62:65], v[18:33]
	ds_read_b128 v[58:61], v202 offset:192
	ds_read_b128 v[62:65], v202 offset:33472
	ds_read_b128 v[54:57], v204 offset:4096
	s_waitcnt lgkmcnt(7)
	v_mfma_f32_32x32x16_f16 v[2:17], v[110:113], v[122:125], v[2:17]
	s_waitcnt vmcnt(2) lgkmcnt(5)
	v_mfma_f32_32x32x16_f16 v[18:33], v[106:109], v[50:53], v[18:33]
	ds_read_b128 v[122:125], v202 offset:224
	ds_read_b128 v[126:129], v202 offset:33504
	ds_read_b128 v[50:53], v204 offset:5120
	s_waitcnt lgkmcnt(7)
	v_mfma_f32_32x32x16_f16 v[2:17], v[106:109], v[118:121], v[2:17]
	s_waitcnt vmcnt(1) lgkmcnt(5)
	v_mfma_f32_32x32x16_f16 v[18:33], v[102:105], v[58:61], v[18:33]
	ds_read_b128 v[114:117], v202 offset:256
	ds_read_b128 v[110:113], v202 offset:33536
	ds_read_b128 v[58:61], v204 offset:6144
	s_waitcnt lgkmcnt(7)
	v_mfma_f32_32x32x16_f16 v[2:17], v[102:105], v[62:65], v[2:17]
	s_waitcnt vmcnt(0) lgkmcnt(5)
	v_mfma_f32_32x32x16_f16 v[18:33], v[98:101], v[122:125], v[18:33]
	ds_read_b128 v[106:109], v202 offset:288
	ds_read_b128 v[102:105], v202 offset:33568
	ds_read_b128 v[62:65], v204 offset:7168
	s_waitcnt lgkmcnt(7)
	v_mfma_f32_32x32x16_f16 v[2:17], v[98:101], v[126:129], v[2:17]
	s_mov_b64 s[6:7], 0x4000
	v_lshl_add_u64 v[98:99], v[174:175], 0, s[6:7]
	s_mov_b64 s[6:7], 0x1000
